# g7 + P.V accumulator chains interleaved (o0/o1 alternate) instead of four dependent MFMAs back to back
# speedup vs baseline: 1.0158x; 1.0105x over previous
; template <bool FIRST> DEVI bool partialSM(f32x16& p0, f32x16& p1, float& m_reg, float& alpha) {
;     float pmax = p0[0];
; #pragma unroll
;     for (int r = 1; r < 16; ++r) pmax = fmaxf(pmax, p0[r]);
; #pragma unroll
;     for (int r = 0; r < 16; ++r) pmax = fmaxf(pmax, p1[r]);
;     { auto rr = __builtin_amdgcn_permlane32_swap(__float_as_uint(pmax), __float_as_uint(pmax), false, false);
;       pmax = fmaxf(__uint_as_float(rr[0]), __uint_as_float(rr[1])); }
;     if (FIRST) { m_reg = pmax; alpha = 1.f;
; #pragma unroll
;         for (int r = 0; r < 16; ++r) { p0[r] = __builtin_amdgcn_exp2f(p0[r] - pmax); p1[r] = p1[r] - pmax; }
;         return false;
;     } else if (__builtin_expect(__all(pmax <= ATT_THR), 1)) { alpha = 1.f;
; #pragma unroll
;         for (int r = 0; r < 16; ++r) p0[r] = __builtin_amdgcn_exp2f(p0[r]);
;         return false;
;     } else { const float d = fmaxf(pmax, 0.f); alpha = __builtin_amdgcn_exp2f(-d); m_reg += d;
; #pragma unroll
;         for (int r = 0; r < 16; ++r) { p0[r] = __builtin_amdgcn_exp2f(p0[r] - d); p1[r] = p1[r] - d; }
;         return true;
;     }
; }
; DEVI void finishSM(f32x16& p0, f32x16& p1, float alpha, float& l_reg, bf16x8& pa0, bf16x8& pa1, bf16x8& pa2, bf16x8& pa3) {
; #pragma unroll
;     for (int r = 0; r < 16; ++r) p1[r] = __builtin_amdgcn_exp2f(p1[r]);
;     f32x2 s2 = (f32x2){p0[0], p0[1]} + (f32x2){p1[0], p1[1]};
; #pragma unroll
;     for (int r = 2; r < 16; r += 2) s2 += (f32x2){p0[r], p0[r + 1]} + (f32x2){p1[r], p1[r + 1]};
;     float ps = s2[0] + s2[1];
;     { auto rr = __builtin_amdgcn_permlane32_swap(__float_as_uint(ps), __float_as_uint(ps), false, false);
;       ps = __uint_as_float(rr[0]) + __uint_as_float(rr[1]); }
;     l_reg = l_reg * alpha + ps;
;     ...
;     PK4(p0, 0, pa0); PK4(p0, 8, pa1); PK4(p1, 0, pa2); PK4(p1, 8, pa3);
;     ...
; }
; DEVI void qkt(f32x16& p0, f32x16& p1, const char* Kb, const bf16x8 (&qr)[6], int r32, int hi, const f32x16& cinit) {
; #pragma unroll
;     for (int d0 = 0; d0 < 6; ++d0) { const int cb = (d0 * 16 + hi * 8) * 2;
;         const bf16x8 k0 = *(const bf16x8*)(Kb + KSWZ(r32, cb)), k1 = *(const bf16x8*)(Kb + KSWZ(32 + r32, cb));
;         p0 = __builtin_amdgcn_mfma_f32_32x32x16_bf16(k0, qr[d0], d0 == 0 ? cinit : p0, 0, 0, 0);
;         p1 = __builtin_amdgcn_mfma_f32_32x32x16_bf16(k1, qr[d0], d0 == 0 ? cinit : p1, 0, 0, 0); }
; }
.LBB0_696:
	v_add_u32_e32 v174, s98, v204
	v_exp_f32_e32 v66, v66
	v_exp_f32_e32 v67, v67
	s_waitcnt lgkmcnt(1)
	v_mfma_f32_32x32x16_bf16 v[98:113], v[82:85], v[150:153], v[34:49]
	v_add_u32_e32 v82, s98, v184
	v_add_u32_e32 v83, s98, v185
	ds_read_b128 v[208:211], v82 offset:12288
	ds_read_b128 v[212:215], v82 offset:18432
	ds_read_b128 v[216:219], v83 offset:12288
	ds_read_b128 v[220:223], v83 offset:18432
	v_exp_f32_e32 v68, v68
	v_exp_f32_e32 v69, v69
	v_exp_f32_e32 v70, v70
	v_exp_f32_e32 v71, v71
	s_waitcnt lgkmcnt(4)
	v_mfma_f32_32x32x16_bf16 v[82:97], v[124:127], v[150:153], v[34:49]
	ds_read_b128 v[124:127], v174 offset:12288
	ds_read_b128 v[224:227], v174 offset:18432
	v_exp_f32_e32 v72, v72
	v_exp_f32_e32 v73, v73
	v_exp_f32_e32 v74, v74
	v_exp_f32_e32 v75, v75
	v_exp_f32_e32 v76, v76
	v_exp_f32_e32 v77, v77
	s_waitcnt lgkmcnt(5)
	v_mfma_f32_32x32x16_bf16 v[98:113], v[208:211], v[138:141], v[98:113]
	v_add_u32_e32 v174, s98, v205
	v_exp_f32_e32 v78, v78
	v_exp_f32_e32 v79, v79
	ds_read_b128 v[228:231], v174 offset:12288
	ds_read_b128 v[232:235], v174 offset:18432
	v_exp_f32_e32 v80, v80
	v_exp_f32_e32 v81, v81
	v_add_u32_e32 v174, s98, v206
	s_waitcnt lgkmcnt(6)
	v_mfma_f32_32x32x16_bf16 v[82:97], v[212:215], v[138:141], v[82:97]
	v_add_f32_e64 v212, v50, v66
	v_add_f32_e64 v213, v51, v67
	v_add_f32_e64 v214, v52, v68
	v_add_f32_e64 v215, v53, v69
	v_lshl_add_u32 v202, s89, 14, v115
	v_pk_add_f32 v[212:213], v[214:215], v[212:213]
	v_pk_add_f32 v[214:215], v[54:55], v[70:71]
	ds_read_b128 v[208:211], v174 offset:12288
	ds_read_b128 v[236:239], v174 offset:18432
	v_pk_add_f32 v[212:213], v[214:215], v[212:213]
	s_waitcnt lgkmcnt(7)
	v_mfma_f32_32x32x16_bf16 v[98:113], v[216:219], v[134:137], v[98:113]
	v_add_f32_e64 v214, v56, v72
	v_add_f32_e64 v215, v57, v73
	v_cvt_pk_bf16_f32 v50, v50, v51
	v_cvt_pk_bf16_f32 v51, v52, v53
	v_cvt_pk_bf16_f32 v52, v54, v55
	v_cvt_pk_bf16_f32 v53, v56, v57
	v_cvt_pk_bf16_f32 v54, v58, v59
	v_add_f32_e64 v212, v214, v212
	v_add_f32_e64 v213, v215, v213
	s_waitcnt lgkmcnt(6)
	v_mfma_f32_32x32x16_bf16 v[82:97], v[220:223], v[134:137], v[82:97]
	v_add_f32_e64 v214, v58, v74
	v_add_f32_e64 v215, v59, v75
	v_cvt_pk_bf16_f32 v55, v60, v61
	v_cvt_pk_bf16_f32 v56, v62, v63
	v_cvt_pk_bf16_f32 v57, v64, v65
	v_cvt_pk_bf16_f32 v58, v66, v67
	v_cvt_pk_bf16_f32 v59, v68, v69
	v_add_f32_e64 v212, v214, v212
	v_add_f32_e64 v213, v215, v213
	s_waitcnt lgkmcnt(5)
	v_mfma_f32_32x32x16_bf16 v[98:113], v[124:127], v[130:133], v[98:113]
	v_add_f32_e64 v214, v60, v76
	v_add_f32_e64 v215, v61, v77
	v_add_f32_e64 v126, v62, v78
	v_add_f32_e64 v127, v63, v79
	v_add_f32_e64 v124, v214, v212
	v_add_f32_e64 v125, v215, v213
	v_cvt_pk_bf16_f32 v60, v70, v71
	v_cvt_pk_bf16_f32 v61, v72, v73
	v_cvt_pk_bf16_f32 v62, v74, v75
	v_cvt_pk_bf16_f32 v63, v76, v77
	s_waitcnt lgkmcnt(4)
	v_mfma_f32_32x32x16_bf16 v[82:97], v[224:227], v[130:133], v[82:97]
	v_add_f32_e64 v124, v126, v124
	v_add_f32_e64 v125, v127, v125
	v_add_f32_e64 v126, v64, v80
	v_add_f32_e64 v127, v65, v81
	v_cvt_pk_bf16_f32 v64, v78, v79
	v_cvt_pk_bf16_f32 v65, v80, v81
	ds_read_b64_tr_b16 v[66:67], v202 offset:0
	ds_read_b64_tr_b16 v[68:69], v202 offset:0x400
	ds_read_b64_tr_b16 v[70:71], v202 offset:0x800
	s_waitcnt lgkmcnt(6)
	v_mfma_f32_32x32x16_bf16 v[98:113], v[228:231], v[146:149], v[98:113]
	ds_read_b64_tr_b16 v[72:73], v202 offset:0xc00
	ds_read_b64_tr_b16 v[74:75], v202 offset:0x1000
	ds_read_b64_tr_b16 v[76:77], v202 offset:0x1400
	ds_read_b64_tr_b16 v[78:79], v202 offset:0x1800
	ds_read_b64_tr_b16 v[80:81], v202 offset:0x1c00
	v_add_f32_e64 v124, v126, v124
	v_add_f32_e64 v125, v127, v125
	s_waitcnt lgkmcnt(10)
	v_mfma_f32_32x32x16_bf16 v[82:97], v[232:235], v[146:149], v[82:97]
	v_pk_add_f32 v[124:125], v[124:125], v[124:125] op_sel:[0,1] op_sel_hi:[1,0]
	s_nop 0
	v_mov_b32_e32 v125, v124
	s_nop 1
	v_permlane32_swap_b32_e32 v124, v125
	s_waitcnt lgkmcnt(9)
	v_mfma_f32_32x32x16_bf16 v[98:113], v[208:211], v[142:145], v[98:113]
	ds_read_b64_tr_b16 v[208:209], v202 offset:0x200
	ds_read_b64_tr_b16 v[210:211], v202 offset:0x600
	ds_read_b64_tr_b16 v[212:213], v202 offset:0xa00
	ds_read_b64_tr_b16 v[214:215], v202 offset:0xe00
	ds_read_b64_tr_b16 v[216:217], v202 offset:0x1200
	ds_read_b64_tr_b16 v[218:219], v202 offset:0x1600
	ds_read_b64_tr_b16 v[220:221], v202 offset:0x1a00
	s_waitcnt lgkmcnt(15)
	v_mfma_f32_32x32x16_bf16 v[82:97], v[236:239], v[142:145], v[82:97]
	ds_read_b64_tr_b16 v[222:223], v202 offset:0x1e00
	s_waitcnt lgkmcnt(14)
	v_mfma_f32_32x32x16_bf16 v[18:33], v[50:53], v[66:69], v[18:33]
	s_waitcnt lgkmcnt(6)
	v_mfma_f32_32x32x16_bf16 v[2:17], v[50:53], v[208:211], v[2:17]
	s_nop 8
	v_max_f32_e32 v249, v99, v99
	v_max_f32_e32 v250, v98, v98
	v_max_f32_e32 v249, v250, v249
	v_max3_f32 v249, v249, v100, v101
	v_max3_f32 v249, v249, v102, v103
	v_max3_f32 v251, v249, v104, v105
	v_max3_f32 v251, v251, v106, v107
	v_exp_f32_e32 v50, v98
	v_exp_f32_e32 v51, v99
	v_exp_f32_e32 v52, v100
	v_exp_f32_e32 v53, v101
	v_mov_b64_e32 v[66:67], v[82:83]
	v_mov_b64_e32 v[68:69], v[84:85]
	v_mfma_f32_32x32x16_bf16 v[18:33], v[54:57], v[70:73], v[18:33]
	s_waitcnt lgkmcnt(4)
	v_mfma_f32_32x32x16_bf16 v[2:17], v[54:57], v[212:215], v[2:17]
	v_max3_f32 v251, v251, v108, v109
	v_max3_f32 v251, v251, v110, v111
	v_max3_f32 v251, v251, v112, v113
	v_max3_f32 v251, v251, v82, v83
	v_max3_f32 v251, v251, v84, v85
	v_max3_f32 v251, v251, v86, v87
	v_max3_f32 v251, v251, v88, v89
	v_exp_f32_e32 v54, v102
	v_exp_f32_e32 v55, v103
	v_exp_f32_e32 v56, v104
	v_exp_f32_e32 v57, v105
	v_mov_b64_e32 v[70:71], v[86:87]
	v_mov_b64_e32 v[72:73], v[88:89]
	v_mfma_f32_32x32x16_bf16 v[18:33], v[58:61], v[74:77], v[18:33]
	s_waitcnt lgkmcnt(2)
	v_mfma_f32_32x32x16_bf16 v[2:17], v[58:61], v[216:219], v[2:17]
	v_max3_f32 v251, v251, v90, v91
	v_max3_f32 v251, v251, v92, v93
	v_max3_f32 v251, v251, v94, v95
	v_max3_f32 v251, v251, v96, v97
	v_mov_b32_e32 v252, v251
	s_nop 1
	v_permlane32_swap_b32_e32 v251, v252
	v_exp_f32_e32 v58, v106
	v_exp_f32_e32 v59, v107
	v_exp_f32_e32 v60, v108
	v_exp_f32_e32 v61, v109
	v_mov_b64_e32 v[74:75], v[90:91]
	v_mov_b64_e32 v[76:77], v[92:93]
	v_mfma_f32_32x32x16_bf16 v[18:33], v[62:65], v[78:81], v[18:33]
	s_waitcnt lgkmcnt(0)
	v_mfma_f32_32x32x16_bf16 v[2:17], v[62:65], v[220:223], v[2:17]
	v_exp_f32_e32 v62, v110
	v_exp_f32_e32 v63, v111
	v_exp_f32_e32 v64, v112
	v_exp_f32_e32 v65, v113
	v_mov_b64_e32 v[78:79], v[94:95]
	v_mov_b64_e32 v[80:81], v[96:97]
	v_max_f32_e32 v252, v252, v252
	v_max_f32_e32 v251, v251, v251
	v_max_f32_e32 v126, v251, v252
	v_cmp_ge_f32_e32 vcc, s79, v126
	s_cmp_lg_u64 vcc, exec
	s_cselect_b64 s[6:7], -1, 0
	s_cbranch_scc1 .LBB0_705
	v_mov_b32_e32 v208, 1.0
	v_mov_b32_e32 v209, v203
	s_branch .LBB0_699

; #define PK4(P, BASE, OUT) do { u32x4 w = {cvt_pk_bf16(P[BASE + 0], P[BASE + 1]), cvt_pk_bf16(P[BASE + 2], P[BASE + 3]), cvt_pk_bf16(P[BASE + 4], P[BASE + 5]), cvt_pk_bf16(P[BASE + 6], P[BASE + 7])}; \
;     OUT = *reinterpret_cast<bf16x8*>(&w); } while (0)
; DEVI void finishSM(f32x16& p0, f32x16& p1, float alpha, float& l_reg, bf16x8& pa0, bf16x8& pa1, bf16x8& pa2, bf16x8& pa3) {
; #pragma unroll
;     for (int r = 0; r < 16; ++r) p1[r] = __builtin_amdgcn_exp2f(p1[r]);
;     f32x2 s2 = (f32x2){p0[0], p0[1]} + (f32x2){p1[0], p1[1]};
; #pragma unroll
;     for (int r = 2; r < 16; r += 2) s2 += (f32x2){p0[r], p0[r + 1]} + (f32x2){p1[r], p1[r + 1]};
;     float ps = s2[0] + s2[1];
;     { auto rr = __builtin_amdgcn_permlane32_swap(__float_as_uint(ps), __float_as_uint(ps), false, false);
;       ps = __uint_as_float(rr[0]) + __uint_as_float(rr[1]); }
;     l_reg = l_reg * alpha + ps;
;     ...
;     PK4(p0, 0, pa0); PK4(p0, 8, pa1); PK4(p1, 0, pa2); PK4(p1, 8, pa3);
;     ...
; }
; DEVI void qkt(f32x16& p0, f32x16& p1, const char* Kb, const bf16x8 (&qr)[6], int r32, int hi, const f32x16& cinit) {
; #pragma unroll
;     for (int d0 = 0; d0 < 6; ++d0) { const int cb = (d0 * 16 + hi * 8) * 2;
;         const bf16x8 k0 = *(const bf16x8*)(Kb + KSWZ(r32, cb)), k1 = *(const bf16x8*)(Kb + KSWZ(32 + r32, cb));
;         p0 = __builtin_amdgcn_mfma_f32_32x32x16_bf16(k0, qr[d0], d0 == 0 ? cinit : p0, 0, 0, 0);
;         p1 = __builtin_amdgcn_mfma_f32_32x32x16_bf16(k1, qr[d0], d0 == 0 ? cinit : p1, 0, 0, 0); }
; }
.LBB0_702:
	s_mul_i32 s98, s2, 0x6000
	s_add_i32 s98, s96, s98
	s_lshl_b32 s99, s2, 14
	s_add_i32 s99, s97, s99
	s_mul_i32 s6, s61, 0x6000
	s_add_i32 s6, s6, 0
	v_add_u32_e32 v86, s6, v129
	v_lshl_add_u64 v[250:251], v[118:119], 0, s[12:13]
	s_mov_b32 m0, s98
	s_barrier
	ds_read_b128 v[82:85], v86
	ds_read_b128 v[210:213], v86 offset:6144
	global_load_lds_dwordx4 v[250:251], off
	v_exp_f32_e32 v66, v66
	s_waitcnt lgkmcnt(1)
	v_mfma_f32_32x32x16_bf16 v[98:113], v[82:85], v[150:153], v[34:49]
	v_add_u32_e32 v126, s6, v184
	v_lshl_add_u64 v[250:251], v[120:121], 0, s[12:13]
	s_add_i32 m0, s98, 0x2000
	v_exp_f32_e32 v67, v67
	v_exp_f32_e32 v68, v68
	global_load_lds_dwordx4 v[250:251], off
	v_exp_f32_e32 v69, v69
	v_exp_f32_e32 v70, v70
	v_exp_f32_e32 v71, v71
	v_exp_f32_e32 v72, v72
	s_waitcnt lgkmcnt(0)
	v_mfma_f32_32x32x16_bf16 v[82:97], v[210:213], v[150:153], v[34:49]
	ds_read_b128 v[210:213], v126
	ds_read_b128 v[214:217], v126 offset:6144
	v_add_u32_e32 v126, s6, v185
	v_lshl_add_u64 v[250:251], v[122:123], 0, s[12:13]
	s_add_i32 m0, s98, 0x4000
	v_exp_f32_e32 v73, v73
	v_exp_f32_e32 v74, v74
	global_load_lds_dwordx4 v[250:251], off
	v_exp_f32_e32 v75, v75
	v_exp_f32_e32 v76, v76
	v_exp_f32_e32 v77, v77
	s_waitcnt lgkmcnt(1)
	v_mfma_f32_32x32x16_bf16 v[98:113], v[210:213], v[138:141], v[98:113]
	s_mov_b32 m0, s99
	v_exp_f32_e32 v78, v78
	v_exp_f32_e32 v79, v79
	v_lshl_add_u64 v[250:251], v[116:117], 0, s[40:41]
	global_load_lds_dwordx4 v[116:117], off
	s_add_i32 m0, s99, 0x2000
	v_exp_f32_e32 v80, v80
	v_exp_f32_e32 v81, v81
	v_add_u32_e32 v174, 0x2000, v202
	global_load_lds_dwordx4 v[250:251], off
	s_waitcnt lgkmcnt(0)
	v_mfma_f32_32x32x16_bf16 v[82:97], v[214:217], v[138:141], v[82:97]
	ds_read_b128 v[210:213], v126
	ds_read_b128 v[214:217], v126 offset:6144
	v_add_u32_e32 v126, s6, v204
	s_waitcnt lgkmcnt(1)
	v_mfma_f32_32x32x16_bf16 v[98:113], v[210:213], v[134:137], v[98:113]
	ds_read_b128 v[210:213], v126
	ds_read_b128 v[218:221], v126 offset:6144
	v_add_u32_e32 v126, s6, v205
	s_waitcnt lgkmcnt(2)
	v_mfma_f32_32x32x16_bf16 v[82:97], v[214:217], v[134:137], v[82:97]
	ds_read_b128 v[214:217], v126
	ds_read_b128 v[222:225], v126 offset:6144
	v_add_u32_e32 v126, s6, v206
	ds_read_b128 v[226:229], v126
	ds_read_b128 v[230:233], v126 offset:6144
	v_pk_add_f32 v[126:127], v[50:51], v[66:67]
	v_cvt_pk_bf16_f32 v50, v50, v51
	v_cvt_pk_bf16_f32 v51, v52, v53
	s_waitcnt lgkmcnt(5)
	v_mfma_f32_32x32x16_bf16 v[98:113], v[210:213], v[130:133], v[98:113]
	v_add_f32_e64 v210, v52, v68
	v_add_f32_e64 v211, v53, v69
	v_cvt_pk_bf16_f32 v52, v54, v55
	v_cvt_pk_bf16_f32 v53, v56, v57
	v_add_f32_e64 v126, v210, v126
	v_add_f32_e64 v127, v211, v127
	v_add_f32_e64 v210, v54, v70
	v_add_f32_e64 v211, v55, v71
	v_cvt_pk_bf16_f32 v54, v58, v59
	s_waitcnt lgkmcnt(4)
	v_mfma_f32_32x32x16_bf16 v[82:97], v[218:221], v[130:133], v[82:97]
	v_add_f32_e64 v126, v210, v126
	v_add_f32_e64 v127, v211, v127
	v_add_f32_e64 v210, v56, v72
	v_add_f32_e64 v211, v57, v73
	v_cvt_pk_bf16_f32 v55, v60, v61
	v_cvt_pk_bf16_f32 v56, v62, v63
	v_cvt_pk_bf16_f32 v57, v64, v65
	v_add_f32_e64 v126, v210, v126
	v_add_f32_e64 v127, v211, v127
	v_pk_add_f32 v[210:211], v[58:59], v[74:75]
	v_cvt_pk_bf16_f32 v58, v66, v67
	v_cvt_pk_bf16_f32 v59, v68, v69
	s_waitcnt lgkmcnt(3)
	v_mfma_f32_32x32x16_bf16 v[98:113], v[214:217], v[146:149], v[98:113]
	v_add_f32_e64 v126, v210, v126
	v_add_f32_e64 v127, v211, v127
	v_add_f32_e64 v210, v60, v76
	v_add_f32_e64 v211, v61, v77
	v_cvt_pk_bf16_f32 v60, v70, v71
	v_cvt_pk_bf16_f32 v61, v72, v73
	v_add_f32_e64 v126, v210, v126
	v_add_f32_e64 v127, v211, v127
	v_pk_add_f32 v[210:211], v[62:63], v[78:79]
	v_cvt_pk_bf16_f32 v62, v74, v75
	v_cvt_pk_bf16_f32 v63, v76, v77
	s_waitcnt lgkmcnt(2)
; DEVI void pv_both(f32x16& o0, f32x16& o1, int vb, bf16x8 pa0, bf16x8 pa1, bf16x8 pa2, bf16x8 pa3) {
;     const s16x4 a0 = tr_read<v_rd_off(0, 0, 0)>(vb), b0 = tr_read<v_rd_off(0, 0, 1)>(vb), a1 = tr_read<v_rd_off(0, 1, 0)>(vb), b1 = tr_read<v_rd_off(0, 1, 1)>(vb);
;     const s16x4 a2 = tr_read<v_rd_off(0, 2, 0)>(vb), b2 = tr_read<v_rd_off(0, 2, 1)>(vb), a3 = tr_read<v_rd_off(0, 3, 0)>(vb), b3 = tr_read<v_rd_off(0, 3, 1)>(vb);
;     const s16x4 c0 = tr_read<v_rd_off(1, 0, 0)>(vb), d0 = tr_read<v_rd_off(1, 0, 1)>(vb), c1 = tr_read<v_rd_off(1, 1, 0)>(vb), d1 = tr_read<v_rd_off(1, 1, 1)>(vb);
;     const s16x4 c2 = tr_read<v_rd_off(1, 2, 0)>(vb), d2 = tr_read<v_rd_off(1, 2, 1)>(vb), c3 = tr_read<v_rd_off(1, 3, 0)>(vb), d3 = tr_read<v_rd_off(1, 3, 1)>(vb);
;     asm volatile("s_waitcnt lgkmcnt(8)" ::: "memory"); SBAR();
;     ...
;     o0 = __builtin_amdgcn_mfma_f32_32x32x16_bf16(pa0, PK(a0, b0), o0, 0, 0, 0);
;     o0 = __builtin_amdgcn_mfma_f32_32x32x16_bf16(pa1, PK(a1, b1), o0, 0, 0, 0);
;     o0 = __builtin_amdgcn_mfma_f32_32x32x16_bf16(pa2, PK(a2, b2), o0, 0, 0, 0);
;     o0 = __builtin_amdgcn_mfma_f32_32x32x16_bf16(pa3, PK(a3, b3), o0, 0, 0, 0);
;     asm volatile("s_waitcnt lgkmcnt(0)" ::: "memory"); SBAR();
;     o1 = __builtin_amdgcn_mfma_f32_32x32x16_bf16(pa0, PK(c0, d0), o1, 0, 0, 0);
;     o1 = __builtin_amdgcn_mfma_f32_32x32x16_bf16(pa1, PK(c1, d1), o1, 0, 0, 0);
;     o1 = __builtin_amdgcn_mfma_f32_32x32x16_bf16(pa2, PK(c2, d2), o1, 0, 0, 0);
;     o1 = __builtin_amdgcn_mfma_f32_32x32x16_bf16(pa3, PK(c3, d3), o1, 0, 0, 0);
;     ...
; }
; template <bool FIRST> DEVI bool partialSM(f32x16& p0, f32x16& p1, float& m_reg, float& alpha) {
;     float pmax = p0[0];
; #pragma unroll
;     for (int r = 1; r < 16; ++r) pmax = fmaxf(pmax, p0[r]);
; #pragma unroll
;     for (int r = 0; r < 16; ++r) pmax = fmaxf(pmax, p1[r]);
;     { auto rr = __builtin_amdgcn_permlane32_swap(__float_as_uint(pmax), __float_as_uint(pmax), false, false);
;       pmax = fmaxf(__uint_as_float(rr[0]), __uint_as_float(rr[1])); }
;     if (FIRST) { m_reg = pmax; alpha = 1.f;
; #pragma unroll
;         for (int r = 0; r < 16; ++r) { p0[r] = __builtin_amdgcn_exp2f(p0[r] - pmax); p1[r] = p1[r] - pmax; }
;         return false;
;     } else if (__builtin_expect(__all(pmax <= ATT_THR), 1)) { alpha = 1.f;
; #pragma unroll
;         for (int r = 0; r < 16; ++r) p0[r] = __builtin_amdgcn_exp2f(p0[r]);
	v_mfma_f32_32x32x16_bf16 v[82:97], v[222:225], v[146:149], v[82:97]
	v_add_f32_e64 v126, v210, v126
	v_add_f32_e64 v127, v211, v127
	v_add_f32_e64 v210, v64, v80
	v_add_f32_e64 v211, v65, v81
	v_cvt_pk_bf16_f32 v64, v78, v79
	v_cvt_pk_bf16_f32 v65, v80, v81
	ds_read_b64_tr_b16 v[66:67], v174 offset:0
	ds_read_b64_tr_b16 v[68:69], v174 offset:0x400
	ds_read_b64_tr_b16 v[70:71], v174 offset:0x800
	ds_read_b64_tr_b16 v[72:73], v174 offset:0xc00
	ds_read_b64_tr_b16 v[74:75], v174 offset:0x1000
	ds_read_b64_tr_b16 v[76:77], v174 offset:0x1400
	ds_read_b64_tr_b16 v[78:79], v174 offset:0x1800
	ds_read_b64_tr_b16 v[80:81], v174 offset:0x1c00
	v_add_f32_e64 v126, v210, v126
	v_add_f32_e64 v127, v211, v127
	ds_read_b64_tr_b16 v[210:211], v174 offset:0x200
	ds_read_b64_tr_b16 v[212:213], v174 offset:0x600
	ds_read_b64_tr_b16 v[214:215], v174 offset:0xa00
	s_waitcnt lgkmcnt(12)
	v_mfma_f32_32x32x16_bf16 v[98:113], v[226:229], v[142:145], v[98:113]
	ds_read_b64_tr_b16 v[216:217], v174 offset:0xe00
	ds_read_b64_tr_b16 v[218:219], v174 offset:0x1200
	ds_read_b64_tr_b16 v[220:221], v174 offset:0x1600
	ds_read_b64_tr_b16 v[222:223], v174 offset:0x1a00
	ds_read_b64_tr_b16 v[224:225], v174 offset:0x1e00
	v_pk_add_f32 v[126:127], v[126:127], v[126:127] op_sel:[0,1] op_sel_hi:[1,0]
	s_waitcnt lgkmcnt(15)
	v_mfma_f32_32x32x16_bf16 v[82:97], v[230:233], v[142:145], v[82:97]
	v_mov_b32_e32 v127, v126
	s_nop 1
	v_permlane32_swap_b32_e32 v126, v127
	s_waitcnt lgkmcnt(14)
	v_mfma_f32_32x32x16_bf16 v[18:33], v[50:53], v[66:69], v[18:33]
	s_waitcnt lgkmcnt(6)
	v_mfma_f32_32x32x16_bf16 v[2:17], v[50:53], v[210:213], v[2:17]
	s_nop 4
	v_max_f32_e32 v249, v99, v99
	v_max_f32_e32 v250, v98, v98
	v_max_f32_e32 v249, v250, v249
	v_max3_f32 v249, v249, v100, v101
	v_max3_f32 v249, v249, v102, v103
	v_max3_f32 v251, v249, v104, v105
	v_max3_f32 v251, v251, v106, v107
	v_exp_f32_e32 v50, v98
	v_exp_f32_e32 v51, v99
	v_exp_f32_e32 v52, v100
	v_exp_f32_e32 v53, v101
	v_mov_b64_e32 v[66:67], v[82:83]
	v_mov_b64_e32 v[68:69], v[84:85]
	v_mfma_f32_32x32x16_bf16 v[18:33], v[54:57], v[70:73], v[18:33]
	s_waitcnt lgkmcnt(4)
	v_mfma_f32_32x32x16_bf16 v[2:17], v[54:57], v[214:217], v[2:17]
	v_max3_f32 v251, v251, v108, v109
	v_max3_f32 v251, v251, v110, v111
	v_max3_f32 v251, v251, v112, v113
	v_max3_f32 v251, v251, v82, v83
	v_max3_f32 v251, v251, v84, v85
	v_max3_f32 v251, v251, v86, v87
	v_max3_f32 v251, v251, v88, v89
	v_exp_f32_e32 v54, v102
	v_exp_f32_e32 v55, v103
	v_exp_f32_e32 v56, v104
	v_exp_f32_e32 v57, v105
	v_mov_b64_e32 v[70:71], v[86:87]
	v_mov_b64_e32 v[72:73], v[88:89]
	v_mfma_f32_32x32x16_bf16 v[18:33], v[58:61], v[74:77], v[18:33]
	s_waitcnt lgkmcnt(2)
	v_mfma_f32_32x32x16_bf16 v[2:17], v[58:61], v[218:221], v[2:17]
	v_max3_f32 v251, v251, v90, v91
	v_max3_f32 v251, v251, v92, v93
	v_max3_f32 v251, v251, v94, v95
	v_max3_f32 v251, v251, v96, v97
	v_mov_b32_e32 v252, v251
	s_nop 1
	v_permlane32_swap_b32_e32 v251, v252
	v_exp_f32_e32 v58, v106
	v_exp_f32_e32 v59, v107
	v_exp_f32_e32 v60, v108
	v_exp_f32_e32 v61, v109
	v_mov_b64_e32 v[74:75], v[90:91]
	v_mov_b64_e32 v[76:77], v[92:93]
	v_mfma_f32_32x32x16_bf16 v[18:33], v[62:65], v[78:81], v[18:33]
	s_waitcnt lgkmcnt(0)
	v_mfma_f32_32x32x16_bf16 v[2:17], v[62:65], v[222:225], v[2:17]
	v_exp_f32_e32 v62, v110
	v_exp_f32_e32 v63, v111
	v_exp_f32_e32 v64, v112
	v_exp_f32_e32 v65, v113
	v_mov_b64_e32 v[78:79], v[94:95]
	v_mov_b64_e32 v[80:81], v[96:97]
	v_max_f32_e32 v252, v252, v252
	v_max_f32_e32 v251, v251, v251
	v_max_f32_e32 v174, v251, v252
	v_cmp_ge_f32_e32 vcc, s79, v174
	s_cmp_lg_u64 vcc, exec
	s_cselect_b64 s[6:7], -1, 0
	s_cbranch_scc1 .LBB0_711
	v_mov_b32_e32 v202, 1.0
	v_mov_b32_e32 v203, v209
	s_branch .LBB0_716

; template <bool FIRST> DEVI bool partialSM(f32x16& p0, f32x16& p1, float& m_reg, float& alpha) {
;     float pmax = p0[0];
; #pragma unroll
;     for (int r = 1; r < 16; ++r) pmax = fmaxf(pmax, p0[r]);
; #pragma unroll
;     for (int r = 0; r < 16; ++r) pmax = fmaxf(pmax, p1[r]);
;     { auto rr = __builtin_amdgcn_permlane32_swap(__float_as_uint(pmax), __float_as_uint(pmax), false, false);
;       pmax = fmaxf(__uint_as_float(rr[0]), __uint_as_float(rr[1])); }
;     if (FIRST) { m_reg = pmax; alpha = 1.f;
; #pragma unroll
;         for (int r = 0; r < 16; ++r) { p0[r] = __builtin_amdgcn_exp2f(p0[r] - pmax); p1[r] = p1[r] - pmax; }
;         return false;
;     } else if (__builtin_expect(__all(pmax <= ATT_THR), 1)) { alpha = 1.f;
; #pragma unroll
;         for (int r = 0; r < 16; ++r) p0[r] = __builtin_amdgcn_exp2f(p0[r]);
;         return false;
;     } else { const float d = fmaxf(pmax, 0.f); alpha = __builtin_amdgcn_exp2f(-d); m_reg += d;
; #pragma unroll
;         for (int r = 0; r < 16; ++r) { p0[r] = __builtin_amdgcn_exp2f(p0[r] - d); p1[r] = p1[r] - d; }
;         return true;
;     }
; }
; DEVI void finishSM(f32x16& p0, f32x16& p1, float alpha, float& l_reg, bf16x8& pa0, bf16x8& pa1, bf16x8& pa2, bf16x8& pa3) {
; #pragma unroll
;     for (int r = 0; r < 16; ++r) p1[r] = __builtin_amdgcn_exp2f(p1[r]);
;     f32x2 s2 = (f32x2){p0[0], p0[1]} + (f32x2){p1[0], p1[1]};
; #pragma unroll
;     for (int r = 2; r < 16; r += 2) s2 += (f32x2){p0[r], p0[r + 1]} + (f32x2){p1[r], p1[r + 1]};
;     float ps = s2[0] + s2[1];
;     { auto rr = __builtin_amdgcn_permlane32_swap(__float_as_uint(ps), __float_as_uint(ps), false, false);
;       ps = __uint_as_float(rr[0]) + __uint_as_float(rr[1]); }
;     l_reg = l_reg * alpha + ps;
;     ...
;     PK4(p0, 0, pa0); PK4(p0, 8, pa1); PK4(p1, 0, pa2); PK4(p1, 8, pa3);
;     ...
; }
; DEVI void qkt(f32x16& p0, f32x16& p1, const char* Kb, const bf16x8 (&qr)[6], int r32, int hi, const f32x16& cinit) {
; #pragma unroll
;     for (int d0 = 0; d0 < 6; ++d0) { const int cb = (d0 * 16 + hi * 8) * 2;
;         const bf16x8 k0 = *(const bf16x8*)(Kb + KSWZ(r32, cb)), k1 = *(const bf16x8*)(Kb + KSWZ(32 + r32, cb));
;         p0 = __builtin_amdgcn_mfma_f32_32x32x16_bf16(k0, qr[d0], d0 == 0 ? cinit : p0, 0, 0, 0);
;         p1 = __builtin_amdgcn_mfma_f32_32x32x16_bf16(k1, qr[d0], d0 == 0 ? cinit : p1, 0, 0, 0); }
; }
.LBB0_2260:
	v_add_u32_e32 v174, s98, v205
	v_exp_f32_e32 v66, v66
	v_exp_f32_e32 v67, v67
	s_waitcnt lgkmcnt(1)
	v_mfma_f32_32x32x16_bf16 v[98:113], v[82:85], v[150:153], v[34:49]
	v_add_u32_e32 v82, s98, v184
	v_add_u32_e32 v83, s98, v185
	ds_read_b128 v[210:213], v82 offset:12288
	ds_read_b128 v[214:217], v82 offset:18432
	ds_read_b128 v[218:221], v83 offset:12288
	ds_read_b128 v[222:225], v83 offset:18432
	v_exp_f32_e32 v68, v68
	v_exp_f32_e32 v69, v69
	v_exp_f32_e32 v70, v70
	v_exp_f32_e32 v71, v71
	s_waitcnt lgkmcnt(4)
	v_mfma_f32_32x32x16_bf16 v[82:97], v[124:127], v[150:153], v[34:49]
	ds_read_b128 v[124:127], v174 offset:12288
	ds_read_b128 v[226:229], v174 offset:18432
	v_exp_f32_e32 v72, v72
	v_exp_f32_e32 v73, v73
	v_exp_f32_e32 v74, v74
	v_exp_f32_e32 v75, v75
	v_exp_f32_e32 v76, v76
	v_exp_f32_e32 v77, v77
	s_waitcnt lgkmcnt(5)
	v_mfma_f32_32x32x16_bf16 v[98:113], v[210:213], v[138:141], v[98:113]
	v_add_u32_e32 v174, s98, v206
	v_exp_f32_e32 v78, v78
	v_exp_f32_e32 v79, v79
	ds_read_b128 v[230:233], v174 offset:12288
	ds_read_b128 v[234:237], v174 offset:18432
	v_exp_f32_e32 v80, v80
	v_exp_f32_e32 v81, v81
	v_add_u32_e32 v174, s98, v207
	s_waitcnt lgkmcnt(6)
	v_mfma_f32_32x32x16_bf16 v[82:97], v[214:217], v[138:141], v[82:97]
	v_add_f32_e64 v214, v50, v66
	v_add_f32_e64 v215, v51, v67
	v_add_f32_e64 v216, v52, v68
	v_add_f32_e64 v217, v53, v69
	v_lshl_add_u32 v203, s71, 14, v115
	v_pk_add_f32 v[214:215], v[216:217], v[214:215]
	v_pk_add_f32 v[216:217], v[54:55], v[70:71]
	ds_read_b128 v[210:213], v174 offset:12288
	ds_read_b128 v[238:241], v174 offset:18432
	v_pk_add_f32 v[214:215], v[216:217], v[214:215]
	s_waitcnt lgkmcnt(7)
	v_mfma_f32_32x32x16_bf16 v[98:113], v[218:221], v[134:137], v[98:113]
	v_add_f32_e64 v216, v56, v72
	v_add_f32_e64 v217, v57, v73
	v_cvt_pk_bf16_f32 v50, v50, v51
	v_cvt_pk_bf16_f32 v51, v52, v53
	v_cvt_pk_bf16_f32 v52, v54, v55
	v_cvt_pk_bf16_f32 v53, v56, v57
	v_cvt_pk_bf16_f32 v54, v58, v59
	v_add_f32_e64 v214, v216, v214
	v_add_f32_e64 v215, v217, v215
	s_waitcnt lgkmcnt(6)
	v_mfma_f32_32x32x16_bf16 v[82:97], v[222:225], v[134:137], v[82:97]
	v_add_f32_e64 v216, v58, v74
	v_add_f32_e64 v217, v59, v75
	v_cvt_pk_bf16_f32 v55, v60, v61
	v_cvt_pk_bf16_f32 v56, v62, v63
	v_cvt_pk_bf16_f32 v57, v64, v65
	v_cvt_pk_bf16_f32 v58, v66, v67
	v_cvt_pk_bf16_f32 v59, v68, v69
	v_add_f32_e64 v214, v216, v214
	v_add_f32_e64 v215, v217, v215
	s_waitcnt lgkmcnt(5)
	v_mfma_f32_32x32x16_bf16 v[98:113], v[124:127], v[130:133], v[98:113]
	v_add_f32_e64 v216, v60, v76
	v_add_f32_e64 v217, v61, v77
	v_add_f32_e64 v126, v62, v78
	v_add_f32_e64 v127, v63, v79
	v_add_f32_e64 v124, v216, v214
	v_add_f32_e64 v125, v217, v215
	v_cvt_pk_bf16_f32 v60, v70, v71
	v_cvt_pk_bf16_f32 v61, v72, v73
	v_cvt_pk_bf16_f32 v62, v74, v75
	v_cvt_pk_bf16_f32 v63, v76, v77
	s_waitcnt lgkmcnt(4)
	v_mfma_f32_32x32x16_bf16 v[82:97], v[226:229], v[130:133], v[82:97]
	v_add_f32_e64 v124, v126, v124
	v_add_f32_e64 v125, v127, v125
	v_add_f32_e64 v126, v64, v80
	v_add_f32_e64 v127, v65, v81
	v_cvt_pk_bf16_f32 v64, v78, v79
	v_cvt_pk_bf16_f32 v65, v80, v81
	ds_read_b64_tr_b16 v[66:67], v203 offset:0
	ds_read_b64_tr_b16 v[68:69], v203 offset:0x400
	ds_read_b64_tr_b16 v[70:71], v203 offset:0x800
	s_waitcnt lgkmcnt(6)
	v_mfma_f32_32x32x16_bf16 v[98:113], v[230:233], v[146:149], v[98:113]
	ds_read_b64_tr_b16 v[72:73], v203 offset:0xc00
	ds_read_b64_tr_b16 v[74:75], v203 offset:0x1000
	ds_read_b64_tr_b16 v[76:77], v203 offset:0x1400
	ds_read_b64_tr_b16 v[78:79], v203 offset:0x1800
	ds_read_b64_tr_b16 v[80:81], v203 offset:0x1c00
	v_add_f32_e64 v124, v126, v124
	v_add_f32_e64 v125, v127, v125
	s_waitcnt lgkmcnt(10)
	v_mfma_f32_32x32x16_bf16 v[82:97], v[234:237], v[146:149], v[82:97]
	v_pk_add_f32 v[124:125], v[124:125], v[124:125] op_sel:[0,1] op_sel_hi:[1,0]
	s_nop 0
	v_mov_b32_e32 v125, v124
	s_nop 1
	v_permlane32_swap_b32_e32 v124, v125
	s_waitcnt lgkmcnt(9)
	v_mfma_f32_32x32x16_bf16 v[98:113], v[210:213], v[142:145], v[98:113]
	ds_read_b64_tr_b16 v[210:211], v203 offset:0x200
	ds_read_b64_tr_b16 v[212:213], v203 offset:0x600
	ds_read_b64_tr_b16 v[214:215], v203 offset:0xa00
	ds_read_b64_tr_b16 v[216:217], v203 offset:0xe00
	ds_read_b64_tr_b16 v[218:219], v203 offset:0x1200
	ds_read_b64_tr_b16 v[220:221], v203 offset:0x1600
	ds_read_b64_tr_b16 v[222:223], v203 offset:0x1a00
	s_waitcnt lgkmcnt(15)
	v_mfma_f32_32x32x16_bf16 v[82:97], v[238:241], v[142:145], v[82:97]
	ds_read_b64_tr_b16 v[224:225], v203 offset:0x1e00
	s_waitcnt lgkmcnt(14)
	v_mfma_f32_32x32x16_bf16 v[18:33], v[50:53], v[66:69], v[18:33]
	s_waitcnt lgkmcnt(6)
	v_mfma_f32_32x32x16_bf16 v[2:17], v[50:53], v[210:213], v[2:17]
	s_nop 8
	v_max_f32_e32 v249, v99, v99
	v_max_f32_e32 v250, v98, v98
	v_max_f32_e32 v249, v250, v249
	v_max3_f32 v249, v249, v100, v101
	v_max3_f32 v249, v249, v102, v103
	v_max3_f32 v251, v249, v104, v105
	v_max3_f32 v251, v251, v106, v107
	v_exp_f32_e32 v50, v98
	v_exp_f32_e32 v51, v99
	v_exp_f32_e32 v52, v100
	v_exp_f32_e32 v53, v101
	v_mov_b64_e32 v[66:67], v[82:83]
	v_mov_b64_e32 v[68:69], v[84:85]
	v_mfma_f32_32x32x16_bf16 v[18:33], v[54:57], v[70:73], v[18:33]
	s_waitcnt lgkmcnt(4)
	v_mfma_f32_32x32x16_bf16 v[2:17], v[54:57], v[214:217], v[2:17]
	v_max3_f32 v251, v251, v108, v109
	v_max3_f32 v251, v251, v110, v111
	v_max3_f32 v251, v251, v112, v113
	v_max3_f32 v251, v251, v82, v83
	v_max3_f32 v251, v251, v84, v85
	v_max3_f32 v251, v251, v86, v87
	v_max3_f32 v251, v251, v88, v89
	v_exp_f32_e32 v54, v102
	v_exp_f32_e32 v55, v103
	v_exp_f32_e32 v56, v104
	v_exp_f32_e32 v57, v105
	v_mov_b64_e32 v[70:71], v[86:87]
	v_mov_b64_e32 v[72:73], v[88:89]
	v_mfma_f32_32x32x16_bf16 v[18:33], v[58:61], v[74:77], v[18:33]
	s_waitcnt lgkmcnt(2)
	v_mfma_f32_32x32x16_bf16 v[2:17], v[58:61], v[218:221], v[2:17]
	v_max3_f32 v251, v251, v90, v91
	v_max3_f32 v251, v251, v92, v93
	v_max3_f32 v251, v251, v94, v95
	v_max3_f32 v251, v251, v96, v97
	v_mov_b32_e32 v252, v251
	s_nop 1
	v_permlane32_swap_b32_e32 v251, v252
	v_exp_f32_e32 v58, v106
	v_exp_f32_e32 v59, v107
	v_exp_f32_e32 v60, v108
	v_exp_f32_e32 v61, v109
	v_mov_b64_e32 v[74:75], v[90:91]
	v_mov_b64_e32 v[76:77], v[92:93]
	v_mfma_f32_32x32x16_bf16 v[18:33], v[62:65], v[78:81], v[18:33]
	s_waitcnt lgkmcnt(0)
	v_mfma_f32_32x32x16_bf16 v[2:17], v[62:65], v[222:225], v[2:17]
	v_exp_f32_e32 v62, v110
	v_exp_f32_e32 v63, v111
	v_exp_f32_e32 v64, v112
	v_exp_f32_e32 v65, v113
	v_mov_b64_e32 v[78:79], v[94:95]
	v_mov_b64_e32 v[80:81], v[96:97]
	v_max_f32_e32 v252, v252, v252
	v_max_f32_e32 v251, v251, v251
	v_max_f32_e32 v126, v251, v252
	v_cmp_ge_f32_e32 vcc, s80, v126
	s_cmp_lg_u64 vcc, exec
	s_cselect_b64 s[6:7], -1, 0
	s_cbranch_scc1 .LBB0_2269
	v_mov_b32_e32 v209, 1.0
	v_mov_b32_e32 v210, v204
	s_branch .LBB0_2263

; #define PK4(P, BASE, OUT) do { u32x4 w = {cvt_pk_bf16(P[BASE + 0], P[BASE + 1]), cvt_pk_bf16(P[BASE + 2], P[BASE + 3]), cvt_pk_bf16(P[BASE + 4], P[BASE + 5]), cvt_pk_bf16(P[BASE + 6], P[BASE + 7])}; \
;     OUT = *reinterpret_cast<bf16x8*>(&w); } while (0)
; DEVI void finishSM(f32x16& p0, f32x16& p1, float alpha, float& l_reg, bf16x8& pa0, bf16x8& pa1, bf16x8& pa2, bf16x8& pa3) {
; #pragma unroll
;     for (int r = 0; r < 16; ++r) p1[r] = __builtin_amdgcn_exp2f(p1[r]);
;     f32x2 s2 = (f32x2){p0[0], p0[1]} + (f32x2){p1[0], p1[1]};
; #pragma unroll
;     for (int r = 2; r < 16; r += 2) s2 += (f32x2){p0[r], p0[r + 1]} + (f32x2){p1[r], p1[r + 1]};
;     float ps = s2[0] + s2[1];
;     { auto rr = __builtin_amdgcn_permlane32_swap(__float_as_uint(ps), __float_as_uint(ps), false, false);
;       ps = __uint_as_float(rr[0]) + __uint_as_float(rr[1]); }
;     l_reg = l_reg * alpha + ps;
;     ...
;     PK4(p0, 0, pa0); PK4(p0, 8, pa1); PK4(p1, 0, pa2); PK4(p1, 8, pa3);
;     ...
; }
; DEVI void qkt(f32x16& p0, f32x16& p1, const char* Kb, const bf16x8 (&qr)[6], int r32, int hi, const f32x16& cinit) {
; #pragma unroll
;     for (int d0 = 0; d0 < 6; ++d0) { const int cb = (d0 * 16 + hi * 8) * 2;
;         const bf16x8 k0 = *(const bf16x8*)(Kb + KSWZ(r32, cb)), k1 = *(const bf16x8*)(Kb + KSWZ(32 + r32, cb));
;         p0 = __builtin_amdgcn_mfma_f32_32x32x16_bf16(k0, qr[d0], d0 == 0 ? cinit : p0, 0, 0, 0);
;         p1 = __builtin_amdgcn_mfma_f32_32x32x16_bf16(k1, qr[d0], d0 == 0 ? cinit : p1, 0, 0, 0); }
; }
.LBB0_2266:
	s_mul_i32 s98, s61, 0x6000
	s_add_i32 s98, s96, s98
	s_lshl_b32 s99, s61, 14
	s_add_i32 s99, s97, s99
	s_mul_i32 s6, s2, 0x6000
	s_add_i32 s6, s6, 0
	v_add_u32_e32 v86, s6, v129
	v_lshl_add_u64 v[250:251], v[118:119], 0, s[12:13]
	s_mov_b32 m0, s98
	s_barrier
	ds_read_b128 v[82:85], v86
	ds_read_b128 v[212:215], v86 offset:6144
	global_load_lds_dwordx4 v[250:251], off
	v_exp_f32_e32 v66, v66
	s_waitcnt lgkmcnt(1)
	v_mfma_f32_32x32x16_bf16 v[98:113], v[82:85], v[150:153], v[34:49]
	v_add_u32_e32 v126, s6, v184
	v_lshl_add_u64 v[250:251], v[120:121], 0, s[12:13]
	s_add_i32 m0, s98, 0x2000
	v_exp_f32_e32 v67, v67
	v_exp_f32_e32 v68, v68
	global_load_lds_dwordx4 v[250:251], off
	v_exp_f32_e32 v69, v69
	v_exp_f32_e32 v70, v70
	v_exp_f32_e32 v71, v71
	v_exp_f32_e32 v72, v72
	s_waitcnt lgkmcnt(0)
	v_mfma_f32_32x32x16_bf16 v[82:97], v[212:215], v[150:153], v[34:49]
	ds_read_b128 v[212:215], v126
	ds_read_b128 v[216:219], v126 offset:6144
	v_add_u32_e32 v126, s6, v185
	v_lshl_add_u64 v[250:251], v[122:123], 0, s[12:13]
	s_add_i32 m0, s98, 0x4000
	v_exp_f32_e32 v73, v73
	v_exp_f32_e32 v74, v74
	global_load_lds_dwordx4 v[250:251], off
	v_exp_f32_e32 v75, v75
	v_exp_f32_e32 v76, v76
	v_exp_f32_e32 v77, v77
	s_waitcnt lgkmcnt(1)
	v_mfma_f32_32x32x16_bf16 v[98:113], v[212:215], v[138:141], v[98:113]
	s_mov_b32 m0, s99
	v_exp_f32_e32 v78, v78
	v_exp_f32_e32 v79, v79
	v_lshl_add_u64 v[250:251], v[116:117], 0, s[40:41]
	global_load_lds_dwordx4 v[116:117], off
	s_add_i32 m0, s99, 0x2000
	v_exp_f32_e32 v80, v80
	v_exp_f32_e32 v81, v81
	v_add_u32_e32 v174, 0x2000, v203
	global_load_lds_dwordx4 v[250:251], off
	s_waitcnt lgkmcnt(0)
	v_mfma_f32_32x32x16_bf16 v[82:97], v[216:219], v[138:141], v[82:97]
	ds_read_b128 v[212:215], v126
	ds_read_b128 v[216:219], v126 offset:6144
	v_add_u32_e32 v126, s6, v205
	s_waitcnt lgkmcnt(1)
	v_mfma_f32_32x32x16_bf16 v[98:113], v[212:215], v[134:137], v[98:113]
	ds_read_b128 v[212:215], v126
	ds_read_b128 v[220:223], v126 offset:6144
	v_add_u32_e32 v126, s6, v206
	s_waitcnt lgkmcnt(2)
	v_mfma_f32_32x32x16_bf16 v[82:97], v[216:219], v[134:137], v[82:97]
	ds_read_b128 v[216:219], v126
	ds_read_b128 v[224:227], v126 offset:6144
	v_add_u32_e32 v126, s6, v207
	ds_read_b128 v[228:231], v126
	ds_read_b128 v[232:235], v126 offset:6144
	v_pk_add_f32 v[126:127], v[50:51], v[66:67]
	v_cvt_pk_bf16_f32 v50, v50, v51
	v_cvt_pk_bf16_f32 v51, v52, v53
	s_waitcnt lgkmcnt(5)
	v_mfma_f32_32x32x16_bf16 v[98:113], v[212:215], v[130:133], v[98:113]
	v_add_f32_e64 v212, v52, v68
	v_add_f32_e64 v213, v53, v69
	v_cvt_pk_bf16_f32 v52, v54, v55
	v_cvt_pk_bf16_f32 v53, v56, v57
	v_add_f32_e64 v126, v212, v126
	v_add_f32_e64 v127, v213, v127
	v_add_f32_e64 v212, v54, v70
	v_add_f32_e64 v213, v55, v71
	v_cvt_pk_bf16_f32 v54, v58, v59
	s_waitcnt lgkmcnt(4)
	v_mfma_f32_32x32x16_bf16 v[82:97], v[220:223], v[130:133], v[82:97]
	v_add_f32_e64 v126, v212, v126
	v_add_f32_e64 v127, v213, v127
	v_add_f32_e64 v212, v56, v72
	v_add_f32_e64 v213, v57, v73
	v_cvt_pk_bf16_f32 v55, v60, v61
	v_cvt_pk_bf16_f32 v56, v62, v63
	v_cvt_pk_bf16_f32 v57, v64, v65
	v_add_f32_e64 v126, v212, v126
	v_add_f32_e64 v127, v213, v127
	v_pk_add_f32 v[212:213], v[58:59], v[74:75]
	v_cvt_pk_bf16_f32 v58, v66, v67
	v_cvt_pk_bf16_f32 v59, v68, v69
	s_waitcnt lgkmcnt(3)
	v_mfma_f32_32x32x16_bf16 v[98:113], v[216:219], v[146:149], v[98:113]
	v_add_f32_e64 v126, v212, v126
	v_add_f32_e64 v127, v213, v127
	v_add_f32_e64 v212, v60, v76
	v_add_f32_e64 v213, v61, v77
	v_cvt_pk_bf16_f32 v60, v70, v71
	v_cvt_pk_bf16_f32 v61, v72, v73
	v_add_f32_e64 v126, v212, v126
	v_add_f32_e64 v127, v213, v127
	v_pk_add_f32 v[212:213], v[62:63], v[78:79]
	v_cvt_pk_bf16_f32 v62, v74, v75
	v_cvt_pk_bf16_f32 v63, v76, v77
	s_waitcnt lgkmcnt(2)
; DEVI void pv_both(f32x16& o0, f32x16& o1, int vb, bf16x8 pa0, bf16x8 pa1, bf16x8 pa2, bf16x8 pa3) {
;     const s16x4 a0 = tr_read<v_rd_off(0, 0, 0)>(vb), b0 = tr_read<v_rd_off(0, 0, 1)>(vb), a1 = tr_read<v_rd_off(0, 1, 0)>(vb), b1 = tr_read<v_rd_off(0, 1, 1)>(vb);
;     const s16x4 a2 = tr_read<v_rd_off(0, 2, 0)>(vb), b2 = tr_read<v_rd_off(0, 2, 1)>(vb), a3 = tr_read<v_rd_off(0, 3, 0)>(vb), b3 = tr_read<v_rd_off(0, 3, 1)>(vb);
;     const s16x4 c0 = tr_read<v_rd_off(1, 0, 0)>(vb), d0 = tr_read<v_rd_off(1, 0, 1)>(vb), c1 = tr_read<v_rd_off(1, 1, 0)>(vb), d1 = tr_read<v_rd_off(1, 1, 1)>(vb);
;     const s16x4 c2 = tr_read<v_rd_off(1, 2, 0)>(vb), d2 = tr_read<v_rd_off(1, 2, 1)>(vb), c3 = tr_read<v_rd_off(1, 3, 0)>(vb), d3 = tr_read<v_rd_off(1, 3, 1)>(vb);
;     asm volatile("s_waitcnt lgkmcnt(8)" ::: "memory"); SBAR();
;     ...
;     o0 = __builtin_amdgcn_mfma_f32_32x32x16_bf16(pa0, PK(a0, b0), o0, 0, 0, 0);
;     o0 = __builtin_amdgcn_mfma_f32_32x32x16_bf16(pa1, PK(a1, b1), o0, 0, 0, 0);
;     o0 = __builtin_amdgcn_mfma_f32_32x32x16_bf16(pa2, PK(a2, b2), o0, 0, 0, 0);
;     o0 = __builtin_amdgcn_mfma_f32_32x32x16_bf16(pa3, PK(a3, b3), o0, 0, 0, 0);
;     asm volatile("s_waitcnt lgkmcnt(0)" ::: "memory"); SBAR();
;     o1 = __builtin_amdgcn_mfma_f32_32x32x16_bf16(pa0, PK(c0, d0), o1, 0, 0, 0);
;     o1 = __builtin_amdgcn_mfma_f32_32x32x16_bf16(pa1, PK(c1, d1), o1, 0, 0, 0);
;     o1 = __builtin_amdgcn_mfma_f32_32x32x16_bf16(pa2, PK(c2, d2), o1, 0, 0, 0);
;     o1 = __builtin_amdgcn_mfma_f32_32x32x16_bf16(pa3, PK(c3, d3), o1, 0, 0, 0);
;     ...
; }
; template <bool FIRST> DEVI bool partialSM(f32x16& p0, f32x16& p1, float& m_reg, float& alpha) {
;     float pmax = p0[0];
; #pragma unroll
;     for (int r = 1; r < 16; ++r) pmax = fmaxf(pmax, p0[r]);
; #pragma unroll
;     for (int r = 0; r < 16; ++r) pmax = fmaxf(pmax, p1[r]);
;     { auto rr = __builtin_amdgcn_permlane32_swap(__float_as_uint(pmax), __float_as_uint(pmax), false, false);
;       pmax = fmaxf(__uint_as_float(rr[0]), __uint_as_float(rr[1])); }
;     if (FIRST) { m_reg = pmax; alpha = 1.f;
; #pragma unroll
;         for (int r = 0; r < 16; ++r) { p0[r] = __builtin_amdgcn_exp2f(p0[r] - pmax); p1[r] = p1[r] - pmax; }
;         return false;
;     } else if (__builtin_expect(__all(pmax <= ATT_THR), 1)) { alpha = 1.f;
; #pragma unroll
;         for (int r = 0; r < 16; ++r) p0[r] = __builtin_amdgcn_exp2f(p0[r]);
	v_mfma_f32_32x32x16_bf16 v[82:97], v[224:227], v[146:149], v[82:97]
	v_add_f32_e64 v126, v212, v126
	v_add_f32_e64 v127, v213, v127
	v_add_f32_e64 v212, v64, v80
	v_add_f32_e64 v213, v65, v81
	v_cvt_pk_bf16_f32 v64, v78, v79
	v_cvt_pk_bf16_f32 v65, v80, v81
	ds_read_b64_tr_b16 v[66:67], v174 offset:0
	ds_read_b64_tr_b16 v[68:69], v174 offset:0x400
	ds_read_b64_tr_b16 v[70:71], v174 offset:0x800
	ds_read_b64_tr_b16 v[72:73], v174 offset:0xc00
	ds_read_b64_tr_b16 v[74:75], v174 offset:0x1000
	ds_read_b64_tr_b16 v[76:77], v174 offset:0x1400
	ds_read_b64_tr_b16 v[78:79], v174 offset:0x1800
	ds_read_b64_tr_b16 v[80:81], v174 offset:0x1c00
	v_add_f32_e64 v126, v212, v126
	v_add_f32_e64 v127, v213, v127
	ds_read_b64_tr_b16 v[212:213], v174 offset:0x200
	ds_read_b64_tr_b16 v[214:215], v174 offset:0x600
	ds_read_b64_tr_b16 v[216:217], v174 offset:0xa00
	s_waitcnt lgkmcnt(12)
	v_mfma_f32_32x32x16_bf16 v[98:113], v[228:231], v[142:145], v[98:113]
	ds_read_b64_tr_b16 v[218:219], v174 offset:0xe00
	ds_read_b64_tr_b16 v[220:221], v174 offset:0x1200
	ds_read_b64_tr_b16 v[222:223], v174 offset:0x1600
	ds_read_b64_tr_b16 v[224:225], v174 offset:0x1a00
	ds_read_b64_tr_b16 v[226:227], v174 offset:0x1e00
	v_pk_add_f32 v[126:127], v[126:127], v[126:127] op_sel:[0,1] op_sel_hi:[1,0]
	s_waitcnt lgkmcnt(15)
	v_mfma_f32_32x32x16_bf16 v[82:97], v[232:235], v[142:145], v[82:97]
	v_mov_b32_e32 v127, v126
	s_nop 1
	v_permlane32_swap_b32_e32 v126, v127
	s_waitcnt lgkmcnt(14)
	v_mfma_f32_32x32x16_bf16 v[18:33], v[50:53], v[66:69], v[18:33]
	s_waitcnt lgkmcnt(6)
	v_mfma_f32_32x32x16_bf16 v[2:17], v[50:53], v[212:215], v[2:17]
	s_nop 4
	v_max_f32_e32 v249, v99, v99
	v_max_f32_e32 v250, v98, v98
	v_max_f32_e32 v249, v250, v249
	v_max3_f32 v249, v249, v100, v101
	v_max3_f32 v249, v249, v102, v103
	v_max3_f32 v251, v249, v104, v105
	v_max3_f32 v251, v251, v106, v107
	v_exp_f32_e32 v50, v98
	v_exp_f32_e32 v51, v99
	v_exp_f32_e32 v52, v100
	v_exp_f32_e32 v53, v101
	v_mov_b64_e32 v[66:67], v[82:83]
	v_mov_b64_e32 v[68:69], v[84:85]
	v_mfma_f32_32x32x16_bf16 v[18:33], v[54:57], v[70:73], v[18:33]
	s_waitcnt lgkmcnt(4)
	v_mfma_f32_32x32x16_bf16 v[2:17], v[54:57], v[216:219], v[2:17]
	v_max3_f32 v251, v251, v108, v109
	v_max3_f32 v251, v251, v110, v111
	v_max3_f32 v251, v251, v112, v113
	v_max3_f32 v251, v251, v82, v83
	v_max3_f32 v251, v251, v84, v85
	v_max3_f32 v251, v251, v86, v87
	v_max3_f32 v251, v251, v88, v89
	v_exp_f32_e32 v54, v102
	v_exp_f32_e32 v55, v103
	v_exp_f32_e32 v56, v104
	v_exp_f32_e32 v57, v105
	v_mov_b64_e32 v[70:71], v[86:87]
	v_mov_b64_e32 v[72:73], v[88:89]
	v_mfma_f32_32x32x16_bf16 v[18:33], v[58:61], v[74:77], v[18:33]
	s_waitcnt lgkmcnt(2)
	v_mfma_f32_32x32x16_bf16 v[2:17], v[58:61], v[220:223], v[2:17]
	v_max3_f32 v251, v251, v90, v91
	v_max3_f32 v251, v251, v92, v93
	v_max3_f32 v251, v251, v94, v95
	v_max3_f32 v251, v251, v96, v97
	v_mov_b32_e32 v252, v251
	s_nop 1
	v_permlane32_swap_b32_e32 v251, v252
	v_exp_f32_e32 v58, v106
	v_exp_f32_e32 v59, v107
	v_exp_f32_e32 v60, v108
	v_exp_f32_e32 v61, v109
	v_mov_b64_e32 v[74:75], v[90:91]
	v_mov_b64_e32 v[76:77], v[92:93]
	v_mfma_f32_32x32x16_bf16 v[18:33], v[62:65], v[78:81], v[18:33]
	s_waitcnt lgkmcnt(0)
	v_mfma_f32_32x32x16_bf16 v[2:17], v[62:65], v[224:227], v[2:17]
	v_exp_f32_e32 v62, v110
	v_exp_f32_e32 v63, v111
	v_exp_f32_e32 v64, v112
	v_exp_f32_e32 v65, v113
	v_mov_b64_e32 v[78:79], v[94:95]
	v_mov_b64_e32 v[80:81], v[96:97]
	v_max_f32_e32 v252, v252, v252
	v_max_f32_e32 v251, v251, v251
	v_max_f32_e32 v174, v251, v252
	v_cmp_ge_f32_e32 vcc, s80, v174
	s_cmp_lg_u64 vcc, exec
	s_cselect_b64 s[6:7], -1, 0
	s_cbranch_scc1 .LBB0_2275
	v_mov_b32_e32 v203, 1.0
	v_mov_b32_e32 v204, v210
	s_branch .LBB0_2280
